# v73 + attention work queue: next item index claimed when an item's KV loop ends (atomic round trip overlaps the output epilogue)
# speedup vs baseline: 1.0068x; 1.0021x over previous
.LBB0_3599:
	v_cvt_f32_u32_e32 v0, s48
	s_mov_b32 s0, 0x3fb8aa3b
	s_mov_b32 s4, 0xc2ce8ed0
	s_mov_b32 s5, 0x42b17218
	v_mul_f32_e32 v0, 0xbe99999a, v0
	v_mul_f32_e32 v2, 0x3fb8aa3b, v0
	v_fma_f32 v3, v0, s0, -v2
	v_rndne_f32_e32 v4, v2
	v_fmac_f32_e32 v3, 0x32a5705f, v0
	v_sub_f32_e32 v2, v2, v4
	v_add_f32_e32 v2, v2, v3
	v_cvt_i32_f32_e32 v4, v4
	v_exp_f32_e32 v2, v2
	s_waitcnt lgkmcnt(1)
	v_add_f32_e32 v3, v58, v59
	v_mul_f32_e32 v5, 0x3fb8aa3b, v3
	v_rndne_f32_e32 v6, v5
	v_ldexp_f32 v2, v2, v4
	v_fma_f32 v4, v3, s0, -v5
	v_fmac_f32_e32 v4, 0x32a5705f, v3
	v_sub_f32_e32 v5, v5, v6
	v_add_f32_e32 v4, v5, v4
	v_exp_f32_e32 v4, v4
	v_cvt_i32_f32_e32 v5, v6
	v_cmp_ngt_f32_e32 vcc, s4, v0
	s_lshl_b32 s92, s48, 3
	s_lshl_b32 s63, s48, 8
	v_cndmask_b32_e32 v2, 0, v2, vcc
	v_cmp_nlt_f32_e32 vcc, s5, v0
	v_ldexp_f32 v4, v4, v5
	v_cmp_eq_u32_e64 s[74:75], 0, v147
	v_cndmask_b32_e32 v0, v234, v2, vcc
	v_mov_b32_e32 v2, 0x3f4ccccd
	v_fmamk_f32 v0, v0, 0xbf19999a, v2
	s_waitcnt lgkmcnt(0)
	v_add_f32_e32 v2, v55, v57
	v_cmp_ngt_f32_e32 vcc, s4, v3
	v_mul_f32_e32 v5, 0x3fb8aa3b, v2
	v_fma_f32 v6, v2, s0, -v5
	v_cndmask_b32_e32 v4, 0, v4, vcc
	v_cmp_nlt_f32_e32 vcc, s5, v3
	s_lshl_b32 s0, s48, 19
	v_rndne_f32_e32 v7, v5
	v_cndmask_b32_e32 v3, v234, v4, vcc
	v_cmp_ngt_f32_e32 vcc, s4, v2
	s_lshl_b32 s4, s48, 7
	s_add_u32 s2, s84, s2
	s_addc_u32 s3, s85, s3
	s_add_u32 s50, s2, 0x20000
	s_addc_u32 s51, s3, 0
	s_add_u32 s72, s2, 0x30000
	s_addc_u32 s73, s3, 0
	s_add_u32 s2, s84, 0x22600000
	s_addc_u32 s3, s85, 0
	v_writelane_b32 v254, s2, 60
	v_fmac_f32_e32 v6, 0x32a5705f, v2
	v_sub_f32_e32 v5, v5, v7
	v_writelane_b32 v254, s3, 61
	s_add_u32 s2, s84, 0x23a00000
	v_writelane_b32 v254, s2, 62
	s_addc_u32 s2, s85, 0
	v_writelane_b32 v254, s2, 63
	s_add_u32 s2, s84, 0x23600000
	v_writelane_b32 v255, s2, 0
	s_addc_u32 s2, s85, 0
	v_writelane_b32 v255, s2, 1
	s_add_u32 s2, s84, 0x38400000
	s_addc_u32 s3, s85, 0
	v_writelane_b32 v255, s2, 2
	v_add_f32_e32 v5, v5, v6
	v_exp_f32_e32 v5, v5
	v_writelane_b32 v255, s3, 3
	s_add_u32 s2, s84, 0x29000000
	s_addc_u32 s3, s85, 0
	v_writelane_b32 v255, s2, 4
	v_cvt_i32_f32_e32 v6, v7
	v_sub_f32_e32 v152, 1.0, v0
	v_writelane_b32 v255, s3, 5
	s_add_u32 s2, s84, 0x2a000000
	v_writelane_b32 v255, s2, 6
	s_addc_u32 s2, s85, 0
	v_writelane_b32 v255, s2, 7
	s_add_u32 s2, s84, 0x2b000000
	v_writelane_b32 v255, s2, 8
	s_addc_u32 s2, s85, 0
	v_writelane_b32 v255, s2, 9
	s_add_u32 s2, s84, 0x23e00000
	s_addc_u32 s3, s85, 0
	v_writelane_b32 v255, s2, 10
	v_ldexp_f32 v4, v5, v6
	v_cndmask_b32_e32 v4, 0, v4, vcc
	v_writelane_b32 v255, s3, 11
	s_add_u32 s2, s84, 0x2c000000
	s_addc_u32 s3, s85, 0
	v_writelane_b32 v255, s2, 12
	s_add_u32 s0, s84, s0
	v_cmp_nlt_f32_e32 vcc, s5, v2
	v_writelane_b32 v255, s3, 13
	s_addc_u32 s2, s85, 0
	s_add_u32 s3, s0, 0x2c200000
	v_writelane_b32 v255, s3, 14
	s_addc_u32 s3, s2, 0
	v_writelane_b32 v255, s3, 15
	v_writelane_b32 v255, s0, 16
	s_add_u32 s0, s0, 0x2c300000
	v_writelane_b32 v255, s0, 17
	v_writelane_b32 v255, s2, 18
	s_addc_u32 s0, s2, 0
	v_writelane_b32 v255, s0, 19
	s_add_u32 s0, s84, 0x27800000
	v_writelane_b32 v255, s0, 20
	s_addc_u32 s0, s85, 0
	v_writelane_b32 v255, s0, 21
	s_add_u32 s0, s84, 0x27000000
	v_writelane_b32 v255, s0, 22
	s_addc_u32 s0, s85, 0
	v_writelane_b32 v255, s0, 23
	s_add_u32 s0, s84, 0x28800000
	v_writelane_b32 v255, s0, 24
	s_addc_u32 s0, s85, 0
	v_writelane_b32 v255, s0, 25
	s_add_u32 s0, s84, 0x28000000
	v_writelane_b32 v255, s0, 26
	s_addc_u32 s0, s85, 0
	s_add_u32 s2, s84, 0x15b00000
	v_writelane_b32 v255, s0, 27
	s_addc_u32 s3, s85, 0
	v_writelane_b32 v255, s2, 28
	s_mov_b32 s5, s93
	v_cndmask_b32_e32 v2, v234, v4, vcc
	v_writelane_b32 v255, s3, 29
	s_add_u32 s2, s84, 0x8d00000
	s_addc_u32 s3, s85, 0
	v_writelane_b32 v255, s2, 30
	s_add_u32 s0, s84, 0x8900100
	v_sub_f32_e32 v2, v3, v2
	v_writelane_b32 v255, s3, 31
	s_mov_b64 s[2:3], 0
	v_writelane_b32 v255, s0, 32
	s_addc_u32 s0, s85, 0
	v_writelane_b32 v254, s2, 55
	v_writelane_b32 v255, s0, 33
	v_add_f32_e32 v148, v0, v2
	v_writelane_b32 v254, s3, 56
	s_lshl_b64 s[2:3], s[92:93], 2
	v_writelane_b32 v255, s2, 34
	v_mov_b32_e32 v149, v148
	s_mov_b32 s56, 0x38400000
	v_writelane_b32 v255, s3, 35
	s_lshl_b64 s[2:3], s[4:5], 2
	v_writelane_b32 v255, s2, 36
	s_movk_i32 s57, 0x80
	s_movk_i32 s58, 0x84
	v_writelane_b32 v255, s3, 37
	v_writelane_b32 v255, s50, 38
	v_readlane_b32 s59, v254, 27
	s_movk_i32 s60, 0x7f
	v_writelane_b32 v255, s51, 39
	v_writelane_b32 v255, s72, 40
	s_mov_b32 s61, 0xff800000
	s_nop 0
	v_writelane_b32 v255, s73, 41
	v_writelane_b32 v255, s74, 42
	s_nop 1
	v_writelane_b32 v255, s75, 43
	v_writelane_b32 v255, s63, 44
	v_writelane_b32 v255, s84, 45
	s_nop 1
	v_writelane_b32 v255, s85, 46
	s_mov_b32 s32, 0
	s_branch .LBB0_3603

.LBB0_3603:
	s_and_saveexec_b64 s[4:5], s[74:75]
	s_cbranch_execz .LBB0_3607
	s_mov_b64 s[8:9], exec
	v_mbcnt_lo_u32_b32 v0, s8, 0
	v_mbcnt_hi_u32_b32 v0, s9, v0
	v_cmp_eq_u32_e32 vcc, 0, v0
	s_and_saveexec_b64 s[6:7], vcc
	s_cbranch_execz .LBB0_3606
	s_cmp_eq_u32 s32, 0
	s_cbranch_scc1 .Lqe_demand
	s_waitcnt vmcnt(0)
	v_mov_b32_e32 v2, v190
	s_mov_b32 s32, 0
	s_branch .LBB0_3606
.Lqe_demand:
	s_bcnt1_i32_b64 s0, s[8:9]
	v_mov_b32_e32 v2, s0
	global_atomic_add v2, v1, v2, s[50:51] sc0

.LBB0_3633:
	s_cmp_lg_u32 s79, 0
	s_cbranch_scc1 .Lqe_skip0
	s_mov_b64 vcc, exec
	s_mov_b64 exec, 1
	v_readlane_b32 s98, v255, 38
	v_readlane_b32 s99, v255, 39
	v_mov_b32_e32 v190, 1
	s_mov_b32 s32, 1
	s_nop 3
	global_atomic_add v190, v1, v190, s[98:99] sc0
	s_mov_b64 exec, vcc
